# MoE gate/up GEMM activation epilogue: 21 v_pk_mul_f32 fed by single-use v_mov copies split into plain v_mul_f32 on the original registers (bit-identical, 21 fewer VALU per unit)
# speedup vs baseline: 1.0169x; 1.0089x over previous
; #define ACT(t) (KBASE(t) <= qlo + QBLK - 1 && KBASE(t) + KVBLK - 1 >= qlo - W + 1)
; #define ACT(t) (KBASE(t) <= qlo + QBLK - 1 && KBASE(t) + KVBLK - 1 >= qlo - W + 1)
; #define ACT(t) (KBASE(t) <= qlo + QBLK - 1 && KBASE(t) + KVBLK - 1 >= qlo - W + 1)
; __device__ __forceinline__ float silu_mul(float g, float u) { return g * __builtin_amdgcn_rcpf(1.f + __builtin_amdgcn_exp2f(-1.4426950408889634f * g)) * u; }
; __device__ __forceinline__ float clamp_f8(float v) { return __builtin_amdgcn_fmed3f(v, -448.f, 448.f); }
; __device__ __forceinline__ unsigned pack4_fp8(f32x4 v, float sc) {
;     int w = 0; w = __builtin_amdgcn_cvt_pk_fp8_f32(clamp_f8(v[0] * sc), clamp_f8(v[1] * sc), w, false); w = __builtin_amdgcn_cvt_pk_fp8_f32(clamp_f8(v[2] * sc), clamp_f8(v[3] * sc), w, true); return (unsigned)w; }
;     __device__ __forceinline__ void operator()(const f32x4 (&acc)[2][2][4][2], const Unit& u, int wr, int wc, int fr, int fq) const {
;         const int row0 = u.pm * BM + wr * 64 + fr, col0 = u.pn * HALF + wc * 32 + 8 * fq;
;         constexpr float DG = 1.f / (F8_SH * F8_SW1);
;         float ss[2][4];
; #pragma unroll
;         for (int ai = 0; ai < 2; ++ai)
; #pragma unroll
;             for (int m = 0; m < 4; ++m) ss[ai][m] = w[row0 + ai * HALF + m * 16] * (F8_SA * DG);
; #pragma unroll
;         for (int ai = 0; ai < 2; ++ai)
; #pragma unroll
;             for (int m = 0; m < 4; ++m) { unsigned char* rowp = ACT + (size_t)(row0 + ai * HALF + m * 16) * 512 + col0; const float sc = ss[ai][m];
;                 const f32x4 g0 = acc[ai][0][m][0] * DG, g1 = acc[ai][0][m][1] * DG, u0 = acc[ai][1][m][0] * sc, u1 = acc[ai][1][m][1] * sc;
;                 f32x4 a0, a1;
; #pragma unroll
;                 for (int i = 0; i < 4; ++i) { a0[i] = silu_mul(g0[i], u0[i]); a1[i] = silu_mul(g1[i], u1[i]); }
;                 u32x2 w_; w_.x = pack4_fp8(a0, 1.f); w_.y = pack4_fp8(a1, 1.f);
;                 *(u32x2*)rowp = w_; }
;     }
.LBB0_1625:
	v_lshl_add_u32 v2, v169, 8, v175
	v_ashrrev_i32_e32 v3, 31, v2
	s_nop 15
	s_nop 15
	s_nop 15
	s_nop 15
	s_nop 15
	v_lshl_add_u64 v[4:5], v[2:3], 2, s[40:41]
	global_load_dword v21, v[4:5], off
	v_or_b32_e32 v32, 16, v2
	v_or_b32_e32 v16, 32, v2
	v_or_b32_e32 v14, 48, v2
	v_ashrrev_i32_e32 v33, 31, v32
	v_ashrrev_i32_e32 v17, 31, v16
	v_ashrrev_i32_e32 v15, 31, v14
	v_lshl_add_u64 v[6:7], v[32:33], 2, s[40:41]
	v_lshl_add_u64 v[18:19], v[16:17], 2, s[40:41]
	v_mov_b32_e32 v23, v150
	v_mov_b32_e32 v24, v154
	v_mov_b32_e32 v25, v146
	v_mov_b32_e32 v150, v159
	v_mov_b32_e32 v146, v155
	v_mov_b32_e32 v29, v148
	v_mov_b32_e32 v148, v157
	v_lshl_add_u64 v[154:155], v[14:15], 2, s[40:41]
	global_load_dword v13, v[4:5], off offset:512
	global_load_dword v157, v[6:7], off
	global_load_dword v9, v[4:5], off offset:576
	s_nop 0
	global_load_dword v7, v[4:5], off offset:640
	global_load_dword v159, v[18:19], off
	s_nop 0
	global_load_dword v19, v[154:155], off
	s_nop 0
	global_load_dword v5, v[4:5], off offset:704
	v_mov_b32_e32 v20, v156
	v_mov_b32_e32 v22, v158
	v_mov_b32_e32 v26, v160
	v_mov_b32_e32 v27, v152
	v_mov_b32_e32 v152, v161
	v_mov_b32_e32 v30, v167
	v_mov_b32_e32 v31, v167
	v_lshl_or_b32 v10, s59, 7, v191
	v_lshlrev_b64 v[2:3], 9, v[2:3]
	v_ashrrev_i32_e32 v11, 31, v10
	v_lshl_add_u64 v[2:3], s[38:39], 0, v[2:3]
	v_lshl_add_u64 v[2:3], v[2:3], 0, v[10:11]
	v_mov_b32_e32 v158, v120
	v_lshlrev_b64 v[16:17], 9, v[16:17]
	v_lshl_add_u64 v[16:17], s[38:39], 0, v[16:17]
	v_lshl_add_u64 v[16:17], v[16:17], 0, v[10:11]
	v_lshlrev_b64 v[14:15], 9, v[14:15]
	v_lshl_add_u64 v[14:15], s[38:39], 0, v[14:15]
	s_waitcnt vmcnt(0)
	v_pk_mul_f32 v[20:21], v[20:21], s[46:47]
	s_nop 0
	v_mov_b32_e32 v169, v21
	v_mul_f32_e32 v4, 0xbfb8aa3b, v20
	v_pk_mul_f32 v[22:23], v[22:23], v[168:169]
	v_pk_mul_f32 v[24:25], v[24:25], v[168:169]
	v_pk_mul_f32 v[150:151], v[150:151], v[168:169]
	v_pk_mul_f32 v[146:147], v[146:147], v[168:169]
	v_exp_f32_e32 v4, v4
	v_mul_f32_e32 v6, 0xbfb8aa3b, v22
	v_mul_f32_e32 v8, 0xbfb8aa3b, v24
	v_mul_f32_e32 v12, 0xbfb8aa3b, v150
	v_mul_f32_e32 v18, 0xbfb8aa3b, v146
	v_exp_f32_e32 v6, v6
	v_exp_f32_e32 v8, v8
	v_exp_f32_e32 v12, v12
	v_exp_f32_e32 v18, v18
	v_pk_mul_f32 v[26:27], v[26:27], v[168:169]
	v_pk_mul_f32 v[152:153], v[152:153], v[168:169]
	v_pk_mul_f32 v[148:149], v[148:149], v[168:169]
	v_mul_f32_e32 v28, 0xbfb8aa3b, v26
	v_mul_f32_e32 v154, 0xbfb8aa3b, v152
	v_add_f32_e32 v4, 1.0, v4
	v_mul_f32_e32 v155, 0xbfb8aa3b, v148
	v_exp_f32_e32 v156, v28
	v_exp_f32_e32 v154, v154
	v_rcp_f32_e32 v28, v4
	v_add_f32_e32 v4, 1.0, v6
	v_add_f32_e32 v6, 1.0, v8
	v_add_f32_e32 v8, 1.0, v12
	v_exp_f32_e32 v155, v155
	v_add_f32_e32 v12, 1.0, v18
	v_rcp_f32_e32 v4, v4
	v_rcp_f32_e32 v8, v8
	v_rcp_f32_e32 v6, v6
	v_rcp_f32_e32 v12, v12
	v_add_f32_e32 v18, 1.0, v156
	v_add_f32_e32 v154, 1.0, v154
	v_add_f32_e32 v155, 1.0, v155
	v_rcp_f32_e32 v18, v18
	v_rcp_f32_e32 v154, v154
	v_mul_f32_e32 v4, v22, v4
	v_mul_f32_e32 v8, v150, v8
	v_rcp_f32_e32 v155, v155
	v_mul_f32_e32 v6, v24, v6
	v_mul_f32_e32 v12, v146, v12
	v_mul_f32_e32 v4, v4, v23
	v_mul_f32_e32 v8, v8, v151
	v_mul_f32_e32 v6, v6, v25
	v_mul_f32_e32 v12, v12, v147
	v_med3_f32 v4, v4, s77, v197
	v_med3_f32 v8, v8, s77, v197
	v_pk_mul_f32 v[20:21], v[20:21], v[28:29]
	v_med3_f32 v6, v6, s77, v197
	v_cvt_pk_fp8_f32 v30, v4, v8
	v_med3_f32 v4, v12, s77, v197
	v_mul_f32_e32 v20, v20, v21
	v_mul_f32_e32 v18, v26, v18
	v_mul_f32_e32 v21, v152, v154
	v_cvt_pk_fp8_f32 v31, v6, v4
	v_mul_f32_e32 v22, v148, v155
	v_mul_f32_e32 v18, v18, v27
	v_mul_f32_e32 v21, v21, v153
	v_mul_f32_e32 v22, v22, v149
	v_med3_f32 v18, v18, s77, v197
	v_med3_f32 v4, v21, s77, v197
	v_med3_f32 v20, v20, s77, v197
	v_cvt_pk_fp8_f32 v30, v18, v4 op_sel:[0,0,1]
	v_med3_f32 v4, v22, s77, v197
	v_mov_b32_e32 v156, v136
	v_cvt_pk_fp8_f32 v31, v20, v4 op_sel:[0,0,1]
	v_pk_mul_f32 v[20:21], v[156:157], s[46:47]
	v_mov_b32_e32 v169, v21
	v_mul_f32_e32 v22, v142, v168
	v_mul_f32_e32 v23, v138, v169
	v_mul_f32_e32 v4, 0xbfb8aa3b, v22
	v_mul_f32_e32 v24, v134, v168
	v_mul_f32_e32 v25, v130, v169
	v_exp_f32_e32 v4, v4
	v_mul_f32_e32 v6, 0xbfb8aa3b, v24
	v_exp_f32_e32 v6, v6
	v_mov_b32_e32 v138, v143
	v_add_f32_e32 v4, 1.0, v4
	v_rcp_f32_e32 v4, v4
	v_add_f32_e32 v6, 1.0, v6
	v_rcp_f32_e32 v6, v6
	v_mov_b32_e32 v130, v135
	v_mul_f32_e32 v4, v22, v4
	v_mul_f32_e32 v4, v4, v23
	v_mul_f32_e32 v6, v24, v6
	v_pk_mul_f32 v[22:23], v[138:139], v[168:169]
	v_mul_f32_e32 v6, v6, v25
	v_mul_f32_e32 v8, 0xbfb8aa3b, v22
	v_exp_f32_e32 v8, v8
	v_mul_f32_e32 v24, v144, v168
	v_mul_f32_e32 v25, v140, v169
	v_pk_mul_f32 v[28:29], v[130:131], v[168:169]
	v_mul_f32_e32 v18, 0xbfb8aa3b, v24
	v_exp_f32_e32 v18, v18
	v_mul_f32_e32 v12, 0xbfb8aa3b, v28
	v_exp_f32_e32 v12, v12
	v_add_f32_e32 v8, 1.0, v8
	v_rcp_f32_e32 v8, v8
	v_add_f32_e32 v18, 1.0, v18
	v_rcp_f32_e32 v18, v18
	v_add_f32_e32 v12, 1.0, v12
	v_rcp_f32_e32 v12, v12
	v_mul_f32_e32 v8, v22, v8
	v_mul_f32_e32 v22, 0xbfb8aa3b, v20
	v_exp_f32_e32 v22, v22
	v_mul_f32_e32 v18, v24, v18
	v_mov_b32_e32 v140, v145
	v_mul_f32_e32 v18, v18, v25
	v_pk_mul_f32 v[24:25], v[140:141], v[168:169]
	v_mul_f32_e32 v8, v8, v23
	v_mul_f32_e32 v12, v28, v12
	v_mov_b32_e32 v23, v132
	v_mul_f32_e32 v28, 0xbfb8aa3b, v24
	v_mov_b32_e32 v132, v137
	global_store_dwordx2 v[2:3], v[30:31], off
	v_mul_f32_e32 v12, v12, v29
	v_add_f32_e32 v22, 1.0, v22
	v_exp_f32_e32 v30, v28
	v_pk_mul_f32 v[28:29], v[132:133], v[168:169]
	v_rcp_f32_e32 v22, v22
	v_mul_f32_e32 v31, 0xbfb8aa3b, v28
	v_exp_f32_e32 v31, v31
	v_med3_f32 v4, v4, s77, v197
	v_pk_mul_f32 v[20:21], v[20:21], v[22:23]
	v_add_f32_e32 v22, 1.0, v30
; #define ACT(t) (KBASE(t) <= qlo + QBLK - 1 && KBASE(t) + KVBLK - 1 >= qlo - W + 1)
; #define ACT(t) (KBASE(t) <= qlo + QBLK - 1 && KBASE(t) + KVBLK - 1 >= qlo - W + 1)
; #define ACT(t) (KBASE(t) <= qlo + QBLK - 1 && KBASE(t) + KVBLK - 1 >= qlo - W + 1)
; __device__ __forceinline__ float silu_mul(float g, float u) { return g * __builtin_amdgcn_rcpf(1.f + __builtin_amdgcn_exp2f(-1.4426950408889634f * g)) * u; }
; __device__ __forceinline__ float clamp_f8(float v) { return __builtin_amdgcn_fmed3f(v, -448.f, 448.f); }
; __device__ __forceinline__ unsigned pack4_fp8(f32x4 v, float sc) {
;     int w = 0; w = __builtin_amdgcn_cvt_pk_fp8_f32(clamp_f8(v[0] * sc), clamp_f8(v[1] * sc), w, false); w = __builtin_amdgcn_cvt_pk_fp8_f32(clamp_f8(v[2] * sc), clamp_f8(v[3] * sc), w, true); return (unsigned)w; }
;     __device__ __forceinline__ void operator()(const f32x4 (&acc)[2][2][4][2], const Unit& u, int wr, int wc, int fr, int fq) const {
;         const int row0 = u.pm * BM + wr * 64 + fr, col0 = u.pn * HALF + wc * 32 + 8 * fq;
;         constexpr float DG = 1.f / (F8_SH * F8_SW1);
;         float ss[2][4];
; #pragma unroll
;         for (int ai = 0; ai < 2; ++ai)
; #pragma unroll
;             for (int m = 0; m < 4; ++m) ss[ai][m] = w[row0 + ai * HALF + m * 16] * (F8_SA * DG);
; #pragma unroll
;         for (int ai = 0; ai < 2; ++ai)
; #pragma unroll
;             for (int m = 0; m < 4; ++m) { unsigned char* rowp = ACT + (size_t)(row0 + ai * HALF + m * 16) * 512 + col0; const float sc = ss[ai][m];
;                 const f32x4 g0 = acc[ai][0][m][0] * DG, g1 = acc[ai][0][m][1] * DG, u0 = acc[ai][1][m][0] * sc, u1 = acc[ai][1][m][1] * sc;
;                 f32x4 a0, a1;
; #pragma unroll
;                 for (int i = 0; i < 4; ++i) { a0[i] = silu_mul(g0[i], u0[i]); a1[i] = silu_mul(g1[i], u1[i]); }
;                 u32x2 w_; w_.x = pack4_fp8(a0, 1.f); w_.y = pack4_fp8(a1, 1.f);
;                 *(u32x2*)rowp = w_; }
;     }
	v_rcp_f32_e32 v22, v22
	v_add_f32_e32 v23, 1.0, v31
	v_rcp_f32_e32 v23, v23
	v_mul_f32_e32 v30, v20, v21
	v_mul_f32_e32 v20, v24, v22
	v_mul_f32_e32 v21, v20, v25
	v_mul_f32_e32 v20, v28, v23
	v_mul_f32_e32 v24, v20, v29
	v_med3_f32 v8, v8, s77, v197
	v_mov_b32_e32 v20, v167
	v_cvt_pk_fp8_f32 v20, v4, v8
	v_med3_f32 v4, v18, s77, v197
	v_med3_f32 v8, v21, s77, v197
	v_lshlrev_b64 v[26:27], 9, v[32:33]
	v_cvt_pk_fp8_f32 v20, v4, v8 op_sel:[0,0,1]
	v_med3_f32 v4, v6, s77, v197
	v_med3_f32 v6, v12, s77, v197
	v_mov_b32_e32 v21, v167
	v_lshl_add_u64 v[26:27], s[38:39], 0, v[26:27]
	v_cvt_pk_fp8_f32 v21, v4, v6
	v_med3_f32 v6, v24, s77, v197
	v_pk_mul_f32 v[24:25], v[158:159], s[46:47]
	v_lshl_add_u64 v[22:23], v[26:27], 0, v[10:11]
	v_mov_b32_e32 v169, v25
	v_mul_f32_e32 v26, v126, v168
	v_mul_f32_e32 v27, v122, v169
	v_med3_f32 v4, v30, s77, v197
	v_mul_f32_e32 v8, 0xbfb8aa3b, v26
	v_exp_f32_e32 v8, v8
	v_cvt_pk_fp8_f32 v21, v4, v6 op_sel:[0,0,1]
	v_mul_f32_e32 v28, v118, v168
	v_mul_f32_e32 v29, v114, v169
	v_add_f32_e32 v4, 1.0, v8
	v_mul_f32_e32 v12, 0xbfb8aa3b, v28
	v_rcp_f32_e32 v4, v4
	v_exp_f32_e32 v12, v12
	v_mov_b32_e32 v122, v127
	global_store_dwordx2 v[22:23], v[20:21], off
	v_pk_mul_f32 v[20:21], v[122:123], v[168:169]
	v_mov_b32_e32 v114, v119
	v_mul_f32_e32 v8, 0xbfb8aa3b, v20
	v_mul_f32_e32 v4, v26, v4
	v_exp_f32_e32 v8, v8
	v_pk_mul_f32 v[22:23], v[114:115], v[168:169]
	v_add_f32_e32 v6, 1.0, v12
	v_mul_f32_e32 v4, v4, v27
	v_mul_f32_e32 v12, 0xbfb8aa3b, v22
	v_exp_f32_e32 v12, v12
	v_mul_f32_e32 v26, v128, v168
	v_mul_f32_e32 v27, v124, v169
	v_add_f32_e32 v8, 1.0, v8
	v_mul_f32_e32 v18, 0xbfb8aa3b, v26
	v_exp_f32_e32 v18, v18
	v_rcp_f32_e32 v8, v8
	v_add_f32_e32 v12, 1.0, v12
	v_rcp_f32_e32 v12, v12
	v_add_f32_e32 v18, 1.0, v18
	v_mul_f32_e32 v8, v20, v8
	v_rcp_f32_e32 v18, v18
	v_mul_f32_e32 v20, 0xbfb8aa3b, v24
	v_rcp_f32_e32 v6, v6
	v_exp_f32_e32 v20, v20
	v_mul_f32_e32 v12, v22, v12
	v_mov_b32_e32 v124, v129
	v_mul_f32_e32 v12, v12, v23
	v_pk_mul_f32 v[22:23], v[124:125], v[168:169]
	v_mul_f32_e32 v8, v8, v21
	v_mul_f32_e32 v18, v26, v18
	v_mov_b32_e32 v21, v116
	v_mul_f32_e32 v26, 0xbfb8aa3b, v22
	v_mov_b32_e32 v116, v121
	v_mul_f32_e32 v6, v28, v6
	v_mul_f32_e32 v18, v18, v27
	v_add_f32_e32 v20, 1.0, v20
	v_exp_f32_e32 v28, v26
	v_pk_mul_f32 v[26:27], v[116:117], v[168:169]
	v_mul_f32_e32 v6, v6, v29
	v_rcp_f32_e32 v20, v20
	v_mul_f32_e32 v29, 0xbfb8aa3b, v26
	v_exp_f32_e32 v29, v29
	v_med3_f32 v4, v4, s77, v197
	v_pk_mul_f32 v[20:21], v[24:25], v[20:21]
	v_add_f32_e32 v24, 1.0, v28
	v_rcp_f32_e32 v24, v24
	v_add_f32_e32 v25, 1.0, v29
	v_rcp_f32_e32 v25, v25
	v_mul_f32_e32 v28, v20, v21
	v_mul_f32_e32 v20, v22, v24
	v_mul_f32_e32 v21, v20, v23
	v_mul_f32_e32 v20, v26, v25
	v_mul_f32_e32 v22, v20, v27
	v_med3_f32 v8, v8, s77, v197
	v_mov_b32_e32 v20, v167
	v_cvt_pk_fp8_f32 v20, v4, v8
	v_med3_f32 v8, v21, s77, v197
	v_med3_f32 v6, v6, s77, v197
	v_med3_f32 v12, v12, s77, v197
	v_mov_b32_e32 v21, v167
	v_cvt_pk_fp8_f32 v21, v6, v12
	v_med3_f32 v4, v18, s77, v197
	v_cvt_pk_fp8_f32 v20, v4, v8 op_sel:[0,0,1]
	v_med3_f32 v4, v28, s77, v197
	v_med3_f32 v6, v22, s77, v197
	v_cvt_pk_fp8_f32 v21, v4, v6 op_sel:[0,0,1]
	v_mov_b32_e32 v18, v104
	v_lshl_add_u64 v[10:11], v[14:15], 0, v[10:11]
	global_store_dwordx2 v[16:17], v[20:21], off
	v_pk_mul_f32 v[16:17], v[18:19], s[46:47]
	v_mov_b32_e32 v169, v17
	v_mul_f32_e32 v18, v110, v168
	v_mul_f32_e32 v19, v106, v169
	v_mul_f32_e32 v4, 0xbfb8aa3b, v18
	v_exp_f32_e32 v4, v4
	v_mul_f32_e32 v20, v102, v168
	v_mul_f32_e32 v21, v98, v169
	v_mov_b32_e32 v106, v111
	v_mul_f32_e32 v6, 0xbfb8aa3b, v20
	v_exp_f32_e32 v6, v6
	v_add_f32_e32 v4, 1.0, v4
	v_rcp_f32_e32 v4, v4
	v_mov_b32_e32 v98, v103
	v_add_f32_e32 v6, 1.0, v6
	v_rcp_f32_e32 v6, v6
	v_mul_f32_e32 v4, v18, v4
	v_mul_f32_e32 v4, v4, v19
	v_pk_mul_f32 v[18:19], v[106:107], v[168:169]
	v_mul_f32_e32 v6, v20, v6
	v_mul_f32_e32 v8, 0xbfb8aa3b, v18
	v_exp_f32_e32 v8, v8
	v_mul_f32_e32 v6, v6, v21
	v_mul_f32_e32 v20, v112, v168
	v_mul_f32_e32 v21, v108, v169
	v_add_f32_e32 v8, 1.0, v8
	v_mul_f32_e32 v24, 0xbfb8aa3b, v20
	v_pk_mul_f32 v[22:23], v[98:99], v[168:169]
	v_rcp_f32_e32 v8, v8
	v_exp_f32_e32 v24, v24
	v_mul_f32_e32 v12, 0xbfb8aa3b, v22
	v_exp_f32_e32 v12, v12
	v_mul_f32_e32 v8, v18, v8
	v_add_f32_e32 v18, 1.0, v24
	v_rcp_f32_e32 v18, v18
	v_add_f32_e32 v12, 1.0, v12
	v_mul_f32_e32 v8, v8, v19
	v_mul_f32_e32 v19, 0xbfb8aa3b, v16
	v_rcp_f32_e32 v12, v12
	v_exp_f32_e32 v19, v19
	v_mul_f32_e32 v18, v20, v18
	v_mov_b32_e32 v108, v113
	v_mul_f32_e32 v24, v18, v21
	v_pk_mul_f32 v[20:21], v[108:109], v[168:169]
	v_mul_f32_e32 v12, v22, v12
	v_add_f32_e32 v18, 1.0, v19
	v_mov_b32_e32 v19, v100
	v_mul_f32_e32 v22, 0xbfb8aa3b, v20
	v_mov_b32_e32 v100, v105
	v_mul_f32_e32 v12, v12, v23
	v_exp_f32_e32 v25, v22
	v_pk_mul_f32 v[22:23], v[100:101], v[168:169]
	v_rcp_f32_e32 v18, v18
	v_mul_f32_e32 v26, 0xbfb8aa3b, v22
	v_exp_f32_e32 v26, v26
	v_med3_f32 v4, v4, s77, v197
	v_pk_mul_f32 v[16:17], v[16:17], v[18:19]
	v_add_f32_e32 v18, 1.0, v25
	v_rcp_f32_e32 v18, v18
	v_add_f32_e32 v19, 1.0, v26
	v_rcp_f32_e32 v19, v19
	v_mul_f32_e32 v25, v16, v17
	v_mul_f32_e32 v16, v20, v18
	v_mul_f32_e32 v17, v16, v21
	v_mul_f32_e32 v16, v22, v19
	v_mul_f32_e32 v18, v16, v23
	v_med3_f32 v8, v8, s77, v197
	v_mov_b32_e32 v16, v167
	v_cvt_pk_fp8_f32 v16, v4, v8
	v_med3_f32 v4, v24, s77, v197
	v_med3_f32 v8, v17, s77, v197
	v_cvt_pk_fp8_f32 v16, v4, v8 op_sel:[0,0,1]
	v_med3_f32 v4, v6, s77, v197
	v_med3_f32 v6, v12, s77, v197
	v_mov_b32_e32 v12, v88
	v_pk_mul_f32 v[12:13], v[12:13], s[46:47]
	v_mov_b32_e32 v17, v167
	v_mov_b32_e32 v169, v13
	v_mul_f32_e32 v14, v94, v168
; #define ACT(t) (KBASE(t) <= qlo + QBLK - 1 && KBASE(t) + KVBLK - 1 >= qlo - W + 1)
; #define ACT(t) (KBASE(t) <= qlo + QBLK - 1 && KBASE(t) + KVBLK - 1 >= qlo - W + 1)
; #define ACT(t) (KBASE(t) <= qlo + QBLK - 1 && KBASE(t) + KVBLK - 1 >= qlo - W + 1)
; __device__ __forceinline__ float silu_mul(float g, float u) { return g * __builtin_amdgcn_rcpf(1.f + __builtin_amdgcn_exp2f(-1.4426950408889634f * g)) * u; }
; __device__ __forceinline__ float clamp_f8(float v) { return __builtin_amdgcn_fmed3f(v, -448.f, 448.f); }
; __device__ __forceinline__ unsigned pack4_fp8(f32x4 v, float sc) {
;     int w = 0; w = __builtin_amdgcn_cvt_pk_fp8_f32(clamp_f8(v[0] * sc), clamp_f8(v[1] * sc), w, false); w = __builtin_amdgcn_cvt_pk_fp8_f32(clamp_f8(v[2] * sc), clamp_f8(v[3] * sc), w, true); return (unsigned)w; }
;     __device__ __forceinline__ void operator()(const f32x4 (&acc)[2][2][4][2], const Unit& u, int wr, int wc, int fr, int fq) const {
;         const int row0 = u.pm * BM + wr * 64 + fr, col0 = u.pn * HALF + wc * 32 + 8 * fq;
;         constexpr float DG = 1.f / (F8_SH * F8_SW1);
;         float ss[2][4];
; #pragma unroll
;         for (int ai = 0; ai < 2; ++ai)
; #pragma unroll
;             for (int m = 0; m < 4; ++m) ss[ai][m] = w[row0 + ai * HALF + m * 16] * (F8_SA * DG);
; #pragma unroll
;         for (int ai = 0; ai < 2; ++ai)
; #pragma unroll
;             for (int m = 0; m < 4; ++m) { unsigned char* rowp = ACT + (size_t)(row0 + ai * HALF + m * 16) * 512 + col0; const float sc = ss[ai][m];
;                 const f32x4 g0 = acc[ai][0][m][0] * DG, g1 = acc[ai][0][m][1] * DG, u0 = acc[ai][1][m][0] * sc, u1 = acc[ai][1][m][1] * sc;
;                 f32x4 a0, a1;
; #pragma unroll
;                 for (int i = 0; i < 4; ++i) { a0[i] = silu_mul(g0[i], u0[i]); a1[i] = silu_mul(g1[i], u1[i]); }
;                 u32x2 w_; w_.x = pack4_fp8(a0, 1.f); w_.y = pack4_fp8(a1, 1.f);
;                 *(u32x2*)rowp = w_; }
;     }
	v_mul_f32_e32 v15, v90, v169
	v_cvt_pk_fp8_f32 v17, v4, v6
	v_mul_f32_e32 v8, 0xbfb8aa3b, v14
	v_exp_f32_e32 v8, v8
	v_med3_f32 v4, v25, s77, v197
	v_med3_f32 v6, v18, s77, v197
	v_cvt_pk_fp8_f32 v17, v4, v6 op_sel:[0,0,1]
	v_add_f32_e32 v4, 1.0, v8
	v_rcp_f32_e32 v4, v4
	v_mul_f32_e32 v18, v86, v168
	v_mul_f32_e32 v19, v82, v169
	v_mov_b32_e32 v82, v87
	v_mul_f32_e32 v20, 0xbfb8aa3b, v18
	v_exp_f32_e32 v20, v20
	v_mul_f32_e32 v4, v14, v4
	v_mul_f32_e32 v4, v4, v15
	v_pk_mul_f32 v[14:15], v[82:83], v[168:169]
	global_store_dwordx2 v[10:11], v[16:17], off
	v_mov_b32_e32 v90, v95
	v_mul_f32_e32 v16, 0xbfb8aa3b, v14
	v_add_f32_e32 v6, 1.0, v20
	v_pk_mul_f32 v[10:11], v[90:91], v[168:169]
	v_exp_f32_e32 v16, v16
	v_rcp_f32_e32 v6, v6
	v_mul_f32_e32 v8, 0xbfb8aa3b, v10
	v_exp_f32_e32 v8, v8
	v_add_f32_e32 v16, 1.0, v16
	v_mul_f32_e32 v6, v18, v6
	v_rcp_f32_e32 v18, v16
	v_add_f32_e32 v8, 1.0, v8
	v_mul_f32_e32 v16, v96, v168
	v_mul_f32_e32 v17, v92, v169
	v_mul_f32_e32 v6, v6, v19
	v_rcp_f32_e32 v8, v8
	v_mul_f32_e32 v19, 0xbfb8aa3b, v16
	v_exp_f32_e32 v19, v19
	v_mov_b32_e32 v92, v97
	v_mul_f32_e32 v8, v10, v8
	v_mul_f32_e32 v8, v8, v11
	v_add_f32_e32 v11, 1.0, v19
	v_mul_f32_e32 v10, v14, v18
	v_rcp_f32_e32 v11, v11
	v_mul_f32_e32 v14, 0xbfb8aa3b, v12
	v_exp_f32_e32 v14, v14
	v_mul_f32_e32 v18, v10, v15
	v_mul_f32_e32 v10, v16, v11
	v_mul_f32_e32 v19, v10, v17
	v_add_f32_e32 v10, 1.0, v14
	v_pk_mul_f32 v[14:15], v[92:93], v[168:169]
	v_mov_b32_e32 v11, v84
	v_mul_f32_e32 v16, 0xbfb8aa3b, v14
	v_mov_b32_e32 v84, v89
	v_exp_f32_e32 v20, v16
	v_pk_mul_f32 v[16:17], v[84:85], v[168:169]
	v_rcp_f32_e32 v10, v10
	v_mul_f32_e32 v21, 0xbfb8aa3b, v16
	v_exp_f32_e32 v21, v21
	v_med3_f32 v4, v4, s77, v197
	v_pk_mul_f32 v[10:11], v[12:13], v[10:11]
	v_add_f32_e32 v12, 1.0, v20
	v_rcp_f32_e32 v12, v12
	v_add_f32_e32 v13, 1.0, v21
	v_rcp_f32_e32 v13, v13
	v_mul_f32_e32 v20, v10, v11
	v_mul_f32_e32 v10, v14, v12
	v_mul_f32_e32 v11, v10, v15
	v_mul_f32_e32 v10, v16, v13
	v_mul_f32_e32 v12, v10, v17
	v_med3_f32 v8, v8, s77, v197
	v_mov_b32_e32 v10, v167
	v_cvt_pk_fp8_f32 v10, v4, v8
	v_med3_f32 v4, v19, s77, v197
	v_med3_f32 v8, v11, s77, v197
	v_med3_f32 v6, v6, s77, v197
	v_med3_f32 v13, v18, s77, v197
	v_mov_b32_e32 v11, v167
	v_cvt_pk_fp8_f32 v11, v6, v13
	v_cvt_pk_fp8_f32 v10, v4, v8 op_sel:[0,0,1]
	v_mov_b32_e32 v8, v72
	v_pk_mul_f32 v[8:9], v[8:9], s[46:47]
	v_med3_f32 v6, v12, s77, v197
	v_mov_b32_e32 v169, v9
	v_med3_f32 v4, v20, s77, v197
	v_mul_f32_e32 v12, v78, v168
	v_mul_f32_e32 v13, v74, v169
	v_cvt_pk_fp8_f32 v11, v4, v6 op_sel:[0,0,1]
	v_mul_f32_e32 v4, 0xbfb8aa3b, v12
	v_mul_f32_e32 v14, v70, v168
	v_mul_f32_e32 v15, v66, v169
	v_exp_f32_e32 v4, v4
	v_mul_f32_e32 v6, 0xbfb8aa3b, v14
	v_exp_f32_e32 v6, v6
	v_add_co_u32_e32 v16, vcc, s62, v2
	v_add_f32_e32 v4, 1.0, v4
	v_rcp_f32_e32 v4, v4
	v_add_f32_e32 v6, 1.0, v6
	v_rcp_f32_e32 v6, v6
	v_addc_co_u32_e32 v17, vcc, 0, v3, vcc
	v_mov_b32_e32 v74, v79
	global_store_dwordx2 v[16:17], v[10:11], off
	v_pk_mul_f32 v[10:11], v[74:75], v[168:169]
	v_mul_f32_e32 v4, v12, v4
	v_mul_f32_e32 v12, 0xbfb8aa3b, v10
	v_mov_b32_e32 v66, v71
	v_mul_f32_e32 v4, v4, v13
	v_mul_f32_e32 v6, v14, v6
	v_exp_f32_e32 v14, v12
	v_pk_mul_f32 v[12:13], v[66:67], v[168:169]
	v_mul_f32_e32 v6, v6, v15
	v_mul_f32_e32 v16, 0xbfb8aa3b, v12
	v_exp_f32_e32 v16, v16
	v_add_f32_e32 v14, 1.0, v14
	v_rcp_f32_e32 v17, v14
	v_add_f32_e32 v14, 1.0, v16
	v_rcp_f32_e32 v16, v14
	v_mul_f32_e32 v14, v80, v168
	v_mul_f32_e32 v15, v76, v169
	v_mul_f32_e32 v10, v10, v17
	v_mul_f32_e32 v18, 0xbfb8aa3b, v14
	v_exp_f32_e32 v18, v18
	v_mul_f32_e32 v17, v10, v11
	v_mul_f32_e32 v10, v12, v16
	v_mul_f32_e32 v12, 0xbfb8aa3b, v8
	v_add_f32_e32 v11, 1.0, v18
	v_rcp_f32_e32 v11, v11
	v_exp_f32_e32 v12, v12
	v_mul_f32_e32 v16, v10, v13
	v_mov_b32_e32 v76, v81
	v_mul_f32_e32 v10, v14, v11
	v_mul_f32_e32 v18, v10, v15
	v_add_f32_e32 v10, 1.0, v12
	v_pk_mul_f32 v[12:13], v[76:77], v[168:169]
	v_mov_b32_e32 v11, v68
	v_mul_f32_e32 v14, 0xbfb8aa3b, v12
	v_mov_b32_e32 v68, v73
	v_exp_f32_e32 v19, v14
	v_pk_mul_f32 v[14:15], v[68:69], v[168:169]
	v_rcp_f32_e32 v10, v10
	v_mul_f32_e32 v20, 0xbfb8aa3b, v14
	v_exp_f32_e32 v20, v20
	v_med3_f32 v4, v4, s77, v197
	v_pk_mul_f32 v[8:9], v[8:9], v[10:11]
	v_add_f32_e32 v10, 1.0, v19
	v_rcp_f32_e32 v10, v10
	v_add_f32_e32 v11, 1.0, v20
	v_rcp_f32_e32 v11, v11
	v_mul_f32_e32 v19, v8, v9
	v_mul_f32_e32 v8, v12, v10
	v_mul_f32_e32 v9, v8, v13
	v_mul_f32_e32 v8, v14, v11
	v_mul_f32_e32 v10, v8, v15
	v_med3_f32 v11, v17, s77, v197
	v_mov_b32_e32 v8, v167
	v_cvt_pk_fp8_f32 v8, v4, v11
	v_med3_f32 v11, v9, s77, v197
	v_med3_f32 v6, v6, s77, v197
	v_med3_f32 v12, v16, s77, v197
	v_mov_b32_e32 v9, v167
	v_cvt_pk_fp8_f32 v9, v6, v12
	v_med3_f32 v4, v18, s77, v197
	v_cvt_pk_fp8_f32 v8, v4, v11 op_sel:[0,0,1]
	v_med3_f32 v4, v19, s77, v197
	v_med3_f32 v6, v10, s77, v197
	v_cvt_pk_fp8_f32 v9, v4, v6 op_sel:[0,0,1]
	v_mov_b32_e32 v6, v56
	v_pk_mul_f32 v[6:7], v[6:7], s[46:47]
	v_mov_b32_e32 v169, v7
	v_mul_f32_e32 v10, v62, v168
	v_mul_f32_e32 v11, v58, v169
; #define ACT(t) (KBASE(t) <= qlo + QBLK - 1 && KBASE(t) + KVBLK - 1 >= qlo - W + 1)
; #define ACT(t) (KBASE(t) <= qlo + QBLK - 1 && KBASE(t) + KVBLK - 1 >= qlo - W + 1)
; #define ACT(t) (KBASE(t) <= qlo + QBLK - 1 && KBASE(t) + KVBLK - 1 >= qlo - W + 1)
; __device__ __forceinline__ float silu_mul(float g, float u) { return g * __builtin_amdgcn_rcpf(1.f + __builtin_amdgcn_exp2f(-1.4426950408889634f * g)) * u; }
; __device__ __forceinline__ float clamp_f8(float v) { return __builtin_amdgcn_fmed3f(v, -448.f, 448.f); }
; __device__ __forceinline__ unsigned pack4_fp8(f32x4 v, float sc) {
;     int w = 0; w = __builtin_amdgcn_cvt_pk_fp8_f32(clamp_f8(v[0] * sc), clamp_f8(v[1] * sc), w, false); w = __builtin_amdgcn_cvt_pk_fp8_f32(clamp_f8(v[2] * sc), clamp_f8(v[3] * sc), w, true); return (unsigned)w; }
;     __device__ __forceinline__ void operator()(const f32x4 (&acc)[2][2][4][2], const Unit& u, int wr, int wc, int fr, int fq) const {
;         const int row0 = u.pm * BM + wr * 64 + fr, col0 = u.pn * HALF + wc * 32 + 8 * fq;
;         constexpr float DG = 1.f / (F8_SH * F8_SW1);
;         float ss[2][4];
; #pragma unroll
;         for (int ai = 0; ai < 2; ++ai)
; #pragma unroll
;             for (int m = 0; m < 4; ++m) ss[ai][m] = w[row0 + ai * HALF + m * 16] * (F8_SA * DG);
; #pragma unroll
;         for (int ai = 0; ai < 2; ++ai)
; #pragma unroll
;             for (int m = 0; m < 4; ++m) { unsigned char* rowp = ACT + (size_t)(row0 + ai * HALF + m * 16) * 512 + col0; const float sc = ss[ai][m];
;                 const f32x4 g0 = acc[ai][0][m][0] * DG, g1 = acc[ai][0][m][1] * DG, u0 = acc[ai][1][m][0] * sc, u1 = acc[ai][1][m][1] * sc;
;                 f32x4 a0, a1;
; #pragma unroll
;                 for (int i = 0; i < 4; ++i) { a0[i] = silu_mul(g0[i], u0[i]); a1[i] = silu_mul(g1[i], u1[i]); }
;                 u32x2 w_; w_.x = pack4_fp8(a0, 1.f); w_.y = pack4_fp8(a1, 1.f);
;                 *(u32x2*)rowp = w_; }
;     }
	v_mul_f32_e32 v4, 0xbfb8aa3b, v10
	v_exp_f32_e32 v4, v4
	v_mul_f32_e32 v12, v54, v168
	v_mul_f32_e32 v13, v50, v169
	v_mov_b32_e32 v58, v63
	v_mul_f32_e32 v14, 0xbfb8aa3b, v12
	v_add_f32_e32 v4, 1.0, v4
	v_exp_f32_e32 v16, v14
	v_rcp_f32_e32 v4, v4
	v_add_co_u32_e32 v14, vcc, s63, v2
	v_add_f32_e32 v16, 1.0, v16
	s_nop 0
	v_addc_co_u32_e32 v15, vcc, 0, v3, vcc
	global_store_dwordx2 v[14:15], v[8:9], off
	v_pk_mul_f32 v[8:9], v[58:59], v[168:169]
	v_mul_f32_e32 v4, v10, v4
	v_mul_f32_e32 v10, 0xbfb8aa3b, v8
	v_mov_b32_e32 v50, v55
	v_rcp_f32_e32 v16, v16
	v_mul_f32_e32 v4, v4, v11
	v_exp_f32_e32 v14, v10
	v_pk_mul_f32 v[10:11], v[50:51], v[168:169]
	v_mul_f32_e32 v12, v12, v16
	v_mul_f32_e32 v15, 0xbfb8aa3b, v10
	v_exp_f32_e32 v15, v15
	v_mul_f32_e32 v16, v12, v13
	v_add_f32_e32 v12, 1.0, v14
	v_rcp_f32_e32 v14, v12
	v_add_f32_e32 v12, 1.0, v15
	v_rcp_f32_e32 v15, v12
	v_mul_f32_e32 v12, v64, v168
	v_mul_f32_e32 v13, v60, v169
	v_mul_f32_e32 v8, v8, v14
	v_mul_f32_e32 v17, 0xbfb8aa3b, v12
	v_exp_f32_e32 v17, v17
	v_mul_f32_e32 v14, v8, v9
	v_mul_f32_e32 v8, v10, v15
	v_mul_f32_e32 v10, 0xbfb8aa3b, v6
	v_add_f32_e32 v9, 1.0, v17
	v_rcp_f32_e32 v9, v9
	v_exp_f32_e32 v10, v10
	v_mul_f32_e32 v15, v8, v11
	v_mov_b32_e32 v60, v65
	v_mul_f32_e32 v8, v12, v9
	v_mul_f32_e32 v17, v8, v13
	v_add_f32_e32 v8, 1.0, v10
	v_pk_mul_f32 v[10:11], v[60:61], v[168:169]
	v_mov_b32_e32 v9, v52
	v_mul_f32_e32 v12, 0xbfb8aa3b, v10
	v_mov_b32_e32 v52, v57
	v_exp_f32_e32 v18, v12
	v_pk_mul_f32 v[12:13], v[52:53], v[168:169]
	v_rcp_f32_e32 v8, v8
	v_mul_f32_e32 v19, 0xbfb8aa3b, v12
	v_exp_f32_e32 v19, v19
	v_med3_f32 v4, v4, s77, v197
	v_pk_mul_f32 v[6:7], v[6:7], v[8:9]
	v_add_f32_e32 v8, 1.0, v18
	v_rcp_f32_e32 v8, v8
	v_add_f32_e32 v9, 1.0, v19
	v_rcp_f32_e32 v9, v9
	v_mul_f32_e32 v18, v6, v7
	v_mul_f32_e32 v6, v10, v8
	v_mul_f32_e32 v7, v6, v11
	v_mul_f32_e32 v6, v12, v9
	v_mul_f32_e32 v8, v6, v13
	v_med3_f32 v9, v14, s77, v197
	v_mov_b32_e32 v6, v167
	v_cvt_pk_fp8_f32 v6, v4, v9
	v_med3_f32 v9, v7, s77, v197
	v_med3_f32 v10, v16, s77, v197
	v_med3_f32 v11, v15, s77, v197
	v_mov_b32_e32 v7, v167
	v_cvt_pk_fp8_f32 v7, v10, v11
	v_med3_f32 v4, v17, s77, v197
	v_cvt_pk_fp8_f32 v6, v4, v9 op_sel:[0,0,1]
	v_med3_f32 v4, v18, s77, v197
	v_med3_f32 v8, v8, s77, v197
	v_cvt_pk_fp8_f32 v7, v4, v8 op_sel:[0,0,1]
	v_mov_b32_e32 v4, v40
	v_pk_mul_f32 v[4:5], v[4:5], s[46:47]
	v_mov_b32_e32 v169, v5
	v_mul_f32_e32 v8, v46, v168
	v_mul_f32_e32 v9, v42, v169
	v_mul_f32_e32 v10, 0xbfb8aa3b, v8
	v_exp_f32_e32 v14, v10
	v_mul_f32_e32 v10, v38, v168
	v_mul_f32_e32 v11, v34, v169
	v_mov_b32_e32 v42, v47
	v_add_f32_e32 v14, 1.0, v14
	v_rcp_f32_e32 v14, v14
	v_mul_f32_e32 v12, 0xbfb8aa3b, v10
	v_exp_f32_e32 v15, v12
	v_add_co_u32_e32 v12, vcc, s65, v2
	v_mov_b32_e32 v34, v39
	s_nop 0
	v_addc_co_u32_e32 v13, vcc, 0, v3, vcc
	global_store_dwordx2 v[12:13], v[6:7], off
	v_mul_f32_e32 v6, v8, v14
	v_mul_f32_e32 v12, v6, v9
	v_pk_mul_f32 v[6:7], v[42:43], v[168:169]
	v_add_f32_e32 v15, 1.0, v15
	v_mul_f32_e32 v8, 0xbfb8aa3b, v6
	v_rcp_f32_e32 v15, v15
	v_exp_f32_e32 v13, v8
	v_pk_mul_f32 v[8:9], v[34:35], v[168:169]
	v_add_co_u32_e32 v2, vcc, 0x16000, v2
	v_mul_f32_e32 v14, 0xbfb8aa3b, v8
	v_exp_f32_e32 v14, v14
	v_mul_f32_e32 v10, v10, v15
	v_mul_f32_e32 v15, v10, v11
	v_add_f32_e32 v10, 1.0, v13
	v_rcp_f32_e32 v13, v10
	v_add_f32_e32 v10, 1.0, v14
	v_rcp_f32_e32 v14, v10
	v_mul_f32_e32 v10, v48, v168
	v_mul_f32_e32 v11, v44, v169
	v_mul_f32_e32 v6, v6, v13
	v_mul_f32_e32 v16, 0xbfb8aa3b, v10
	v_exp_f32_e32 v16, v16
	v_mul_f32_e32 v13, v6, v7
	v_mul_f32_e32 v6, v8, v14
	v_mul_f32_e32 v8, 0xbfb8aa3b, v4
	v_add_f32_e32 v7, 1.0, v16
	v_rcp_f32_e32 v7, v7
	v_exp_f32_e32 v8, v8
	v_mul_f32_e32 v14, v6, v9
	v_mov_b32_e32 v44, v49
	v_mul_f32_e32 v6, v10, v7
	v_mul_f32_e32 v16, v6, v11
	v_add_f32_e32 v6, 1.0, v8
	v_pk_mul_f32 v[8:9], v[44:45], v[168:169]
	v_mov_b32_e32 v7, v36
	v_mul_f32_e32 v10, 0xbfb8aa3b, v8
	v_mov_b32_e32 v36, v41
	v_exp_f32_e32 v17, v10
	v_pk_mul_f32 v[10:11], v[36:37], v[168:169]
	v_rcp_f32_e32 v6, v6
	v_mul_f32_e32 v18, 0xbfb8aa3b, v10
	v_exp_f32_e32 v18, v18
	v_addc_co_u32_e32 v3, vcc, 0, v3, vcc
	v_pk_mul_f32 v[4:5], v[4:5], v[6:7]
	v_add_f32_e32 v6, 1.0, v17
	v_rcp_f32_e32 v6, v6
	v_add_f32_e32 v7, 1.0, v18
	v_rcp_f32_e32 v7, v7
	v_mul_f32_e32 v17, v4, v5
	v_mul_f32_e32 v4, v8, v6
	v_mul_f32_e32 v5, v4, v9
	v_mul_f32_e32 v4, v10, v7
	v_mul_f32_e32 v6, v4, v11
	v_med3_f32 v7, v12, s77, v197
	v_med3_f32 v8, v13, s77, v197
	v_mov_b32_e32 v4, v167
	v_cvt_pk_fp8_f32 v4, v7, v8
	v_med3_f32 v8, v5, s77, v197
	v_med3_f32 v9, v15, s77, v197
	v_med3_f32 v10, v14, s77, v197
	v_mov_b32_e32 v5, v167
	v_cvt_pk_fp8_f32 v5, v9, v10
	v_med3_f32 v7, v16, s77, v197
	v_cvt_pk_fp8_f32 v4, v7, v8 op_sel:[0,0,1]
	v_med3_f32 v7, v17, s77, v197
	v_med3_f32 v6, v6, s77, v197
	v_cvt_pk_fp8_f32 v5, v7, v6 op_sel:[0,0,1]
	s_and_b64 vcc, exec, s[6:7]
	s_mov_b64 s[6:7], -1
	global_store_dwordx2 v[2:3], v[4:5], off
	s_cbranch_vccnz .LBB0_1613
	s_andn2_b64 vcc, exec, s[24:25]
	s_cbranch_vccnz .LBB0_1612
	s_barrier
	s_branch .LBB0_1612
